# attention phases: static s_setprio 1 for waves 4..7 (one wave of each SIMD pair takes the MFMA pipe first)
# speedup vs baseline: 1.0027x; 1.0027x over previous
.LBB0_466:
	v_readlane_b32 s32, v254, 41
	s_nop 3
	s_cmp_lt_u32 s32, 4
	s_cbranch_scc1 .Lprio_0
	s_setprio 1

.LBB0_517:
	s_setprio 0
	v_readlane_b32 s12, v254, 1
	v_readlane_b32 s13, v254, 2
	s_cmp_lt_i32 s13, 5
	v_readlane_b32 s14, v254, 3
	v_readlane_b32 s15, v254, 4
	s_cbranch_scc1 .LBB0_571
	s_waitcnt vmcnt(0)
	s_barrier
	s_mov_b64 s[0:1], exec
	v_readlane_b32 s2, v254, 39
	v_readlane_b32 s3, v254, 40
	s_and_b64 s[2:3], s[0:1], s[2:3]
	s_mov_b64 exec, s[2:3]
	s_cbranch_execz .LBB0_570
	s_add_i32 s2, 0, 0x24000
	v_mov_b32_e32 v0, s2
	s_waitcnt vmcnt(0) expcnt(0) lgkmcnt(0)
	ds_read_b32 v2, v0
	s_add_i32 s2, 0, 0x24004
	v_mov_b32_e32 v0, s2
	ds_read_b32 v0, v0
	s_waitcnt lgkmcnt(1)
	v_cmp_ne_u32_e32 vcc, 0, v2
	s_cbranch_vccnz .LBB0_534
	v_readlane_b32 s2, v254, 42
	v_readlane_b32 s3, v254, 43
	s_load_dwordx2 s[6:7], s[2:3], 0x4
	s_add_u32 s2, s72, 0x1000
	s_addc_u32 s3, s73, 0
	s_add_u32 s4, s72, 0x1100
	s_addc_u32 s5, s73, 0
	s_waitcnt lgkmcnt(0)
	s_mul_i32 s16, s6, s74
	s_add_u32 s6, s72, 0x1200
	s_mul_i32 s16, s16, s7
	s_addc_u32 s7, s73, 0
	s_add_u32 s8, s72, 0x1300
	s_addc_u32 s9, s73, 0
	s_mov_b32 s17, 1
	v_mov_b32_e32 v16, 0
	s_branch .LBB0_522

.LBB0_1429:
	s_setprio 0
	v_readlane_b32 s12, v254, 1
	v_readlane_b32 s13, v254, 2
	s_cmp_lt_i32 s13, 15
	v_readlane_b32 s14, v254, 3
	v_readlane_b32 s15, v254, 4
	s_cbranch_scc1 .LBB0_1483
	s_waitcnt vmcnt(0)
	s_barrier
	s_mov_b64 s[0:1], exec
	v_readlane_b32 s2, v254, 39
	v_readlane_b32 s3, v254, 40
	s_and_b64 s[2:3], s[0:1], s[2:3]
	s_mov_b64 exec, s[2:3]
	s_cbranch_execz .LBB0_1482
	s_add_i32 s2, 0, 0x24000
	v_mov_b32_e32 v0, s2
	s_waitcnt vmcnt(0) expcnt(0) lgkmcnt(0)
	ds_read_b32 v2, v0
	s_add_i32 s2, 0, 0x24004
	v_mov_b32_e32 v0, s2
	ds_read_b32 v0, v0
	s_waitcnt lgkmcnt(1)
	v_cmp_ne_u32_e32 vcc, 0, v2
	s_cbranch_vccnz .LBB0_1446
	v_readlane_b32 s2, v254, 42
	v_readlane_b32 s3, v254, 43
	s_load_dwordx2 s[6:7], s[2:3], 0x4
	s_add_u32 s2, s72, 0x1000
	s_addc_u32 s3, s73, 0
	s_add_u32 s4, s72, 0x1100
	s_addc_u32 s5, s73, 0
	s_waitcnt lgkmcnt(0)
	s_mul_i32 s16, s6, s74
	s_add_u32 s6, s72, 0x1200
	s_mul_i32 s16, s16, s7
	s_addc_u32 s7, s73, 0
	s_add_u32 s8, s72, 0x1300
	s_addc_u32 s9, s73, 0
	s_mov_b32 s17, 1
	v_mov_b32_e32 v16, 0
	s_branch .LBB0_1434

.LBB0_2307:
	s_setprio 0
	v_readlane_b32 s72, v254, 56
	v_readlane_b32 s12, v254, 1
	v_readlane_b32 s73, v254, 57
	v_readlane_b32 s13, v254, 2
	v_readlane_b32 s14, v254, 3
	v_readlane_b32 s15, v254, 4

.LBB0_3056:
	s_setprio 0
	s_cmp_lt_i32 s85, 35
	s_cbranch_scc1 .LBB0_3110
	s_waitcnt vmcnt(0)
	s_barrier
	s_mov_b64 s[0:1], exec
	v_readlane_b32 s2, v254, 39
	v_readlane_b32 s3, v254, 40
	s_and_b64 s[2:3], s[0:1], s[2:3]
	s_mov_b64 exec, s[2:3]
	s_cbranch_execz .LBB0_3109
	s_add_i32 s2, 0, 0x24000
	v_mov_b32_e32 v0, s2
	s_waitcnt vmcnt(0) expcnt(0) lgkmcnt(0)
	ds_read_b32 v2, v0
	s_add_i32 s2, 0, 0x24004
	v_mov_b32_e32 v0, s2
	ds_read_b32 v0, v0
	s_waitcnt lgkmcnt(1)
	v_cmp_ne_u32_e32 vcc, 0, v2
	s_cbranch_vccnz .LBB0_3073
	v_readlane_b32 s2, v254, 42
	v_readlane_b32 s3, v254, 43
	s_load_dwordx2 s[6:7], s[2:3], 0x4
	s_add_u32 s2, s72, 0x1000
	s_addc_u32 s3, s73, 0
	s_add_u32 s4, s72, 0x1100
	s_addc_u32 s5, s73, 0
	s_waitcnt lgkmcnt(0)
	s_mul_i32 s16, s6, s74
	s_add_u32 s6, s72, 0x1200
	s_mul_i32 s16, s16, s7
	s_addc_u32 s7, s73, 0
	s_add_u32 s8, s72, 0x1300
	s_addc_u32 s9, s73, 0
	s_mov_b32 s17, 1
	v_mov_b32_e32 v16, 0
	s_branch .LBB0_3061
